# speedup vs baseline: 1.0079x; 1.0079x over previous
.LBB2_12:
	s_or_b64 exec, exec, s[12:13]
	v_lshlrev_b32_e32 v106, 9, v119
	v_ffbl_b32_e32 v107, v107
	v_ffbl_b32_e32 v108, v108
	v_lshlrev_b32_e32 v116, 25, v119
	v_lshl_or_b32 v107, v107, 4, v106
	v_mov_b32_e32 v109, 0x2000
	v_lshl_or_b32 v108, v108, 20, v116
	v_bfrev_b32_e32 v116, 4
	v_ffbl_b32_e32 v0, v0
	v_cndmask_b32_e64 v107, v107, v109, s[8:9]
	v_cndmask_b32_e64 v108, v108, v116, s[4:5]
	v_lshl_or_b32 v0, v0, 4, v106
	v_cndmask_b32_e32 v0, v0, v109, vcc
	v_or_b32_e32 v106, v108, v107
	v_mov_b32_e32 v108, 0x800000
	v_lshlrev_b32_e32 v107, 16, v117
	v_cndmask_b32_e64 v108, 0, v108, s[6:7]
	s_waitcnt lgkmcnt(2)
	v_lshl_or_b32 v0, v118, 24, v0
	v_or3_b32 v0, v0, v108, v107
	ds_write2_b32 v105, v106, v0 offset0:1 offset1:3
	v_cmp_ne_u32_e32 vcc, 0, v140
	v_cmp_ne_u32_e64 s[22:23], 0, v141
	v_lshlrev_b32_e32 v150, 5, v113
	v_lshl_add_u32 v155, v113, 2, v115
	v_lshlrev_b32_e32 v155, 2, v155
	v_add_u32_e32 v155, 0x11840, v155
	v_lshrrev_b64 v[146:147], v150, vcc
	v_lshrrev_b64 v[156:157], v150, s[22:23]
	v_mov_b32_e32 v151, 0x400
	v_cmp_ne_u32_e32 vcc, 0, v146
	v_cmp_ne_u32_e64 s[22:23], 0, v156
	s_nop 1
	v_cndmask_b32_e32 v146, 0, v151, vcc
	v_cndmask_b32_e64 v156, 0, v151, s[22:23]
	v_cmp_eq_u32_e32 vcc, 0, v111
	s_and_saveexec_b64 s[22:23], vcc
	ds_or_b32 v155, v146
	ds_or_b32 v155, v156 offset:32
	s_or_b64 exec, exec, s[22:23]
	s_movk_i32 s2, 0x2010
	v_mul_u32_u24_e32 v105, 0x2010, v115
	v_cmp_eq_u32_e32 vcc, 0, v114
	s_waitcnt vmcnt(22)
	ds_write_b128 v104, v[38:41] offset:32832
	s_waitcnt vmcnt(21)
	ds_write_b128 v104, v[42:45] offset:36928
	s_waitcnt vmcnt(20)
	ds_write_b128 v104, v[46:49] offset:41024
	s_waitcnt vmcnt(19)
	ds_write_b128 v104, v[50:53] offset:45120
	s_waitcnt vmcnt(18)
	ds_write_b128 v104, v[54:57] offset:49216
	s_waitcnt vmcnt(17)
	ds_write_b128 v104, v[66:69] offset:53312
	s_and_saveexec_b64 s[0:1], vcc
	v_mov_b32_e32 v38, 0
	v_mov_b32_e32 v39, v38
	v_mov_b32_e32 v40, v38
	v_mov_b32_e32 v41, v38
	ds_write_b128 v105, v[38:41] offset:8192
	s_or_b64 exec, exec, s[0:1]
	v_lshlrev_b32_e32 v40, 3, v113
	v_lshlrev_b32_e32 v67, 4, v110
	v_or_b32_e32 v38, 0x1e0, v111
	v_or_b32_e32 v0, 0x8040, v40
	v_mad_u32_u24 v66, v1, s2, v67
	v_mad_u32_u24 v38, v38, 48, v0
	s_waitcnt vmcnt(16)
	ds_write_b128 v66, v[58:61]
	s_waitcnt vmcnt(15)
	ds_write_b128 v66, v[62:65] offset:1024
	s_waitcnt vmcnt(14)
	ds_write_b128 v66, v[70:73] offset:2048
	s_waitcnt vmcnt(13)
	ds_write_b128 v66, v[74:77] offset:3072
	s_waitcnt vmcnt(12)
	ds_write_b128 v66, v[78:81] offset:4096
	s_waitcnt vmcnt(11)
	ds_write_b128 v66, v[82:85] offset:5120
	s_waitcnt vmcnt(10)
	ds_write_b128 v66, v[86:89] offset:6144
	s_waitcnt vmcnt(9)
	ds_write_b128 v66, v[90:93] offset:7168
	v_lshl_add_u32 v116, v113, 3, v105
	v_or_b32_e32 v106, 0x1e0, v111
	v_lshlrev_b32_e32 v138, 4, v106
	v_lshlrev_b32_e32 v139, 3, v106
	v_add_u32_e32 v139, 0x118c0, v139
	v_mul_u32_u24_e32 v156, 48, v106
	v_add_u32_e32 v156, v0, v156
	v_mov_b32_e32 v157, 0x1187c
	v_add_u32_e32 v137, v116, v138
	v_add_u32_e32 v138, 0x200, v138
	v_lshlrev_b32_e32 v160, 4, v111
	v_lshlrev_b32_e32 v161, 3, v111
	v_add_u32_e32 v161, 0x118c0, v161
	v_mul_u32_u24_e32 v162, 48, v111
	v_add_u32_e32 v162, v0, v162
	v_mov_b32_e32 v163, 0x11840
	v_mul_hi_u32_u24_e32 v159, 0x410, v111
	v_mul_u32_u24_e32 v158, 0x410, v111
	v_mov_b32_e32 v107, 0x82000
	v_mad_u64_u32 v[158:159], s[0:1], s20, v107, v[158:159]
	v_lshlrev_b32_e32 v107, 3, v113
	v_or_b32_e32 v158, v158, v107
	v_lshl_add_u64 v[158:159], s[14:15], 0, v[158:159]
	s_mov_b64 s[0:1], 0x79e30
	s_mov_b32 s2, 0xffff7e00
	s_mov_b32 s3, -1
	v_lshl_add_u64 v[158:159], v[158:159], 0, s[0:1]
	v_lshl_add_u32 v107, v114, 2, v163
	v_add_u32_e32 v107, -8, v107
	s_waitcnt lgkmcnt(0)
	s_barrier
	ds_read_b128 v[38:41], v138 offset:56896
	ds_read_b64 v[42:43], v139
	ds_read2_b64 v[56:59], v156 offset1:2
	ds_read_b32 v60, v107
	v_add_u32_e32 v156, 0xfffffa00, v156
	ds_read2_b64 v[52:55], v156 offset1:2
	v_add_u32_e32 v106, -2, v114
	v_cmp_gt_u32_e32 vcc, 16, v106
	s_waitcnt lgkmcnt(0)
	v_cndmask_b32_e32 v60, 0, v60, vcc
	s_nop 1
	v_readlane_b32 s4, v60, 17
	v_readlane_b32 s21, v60, 16
	v_add_u32_sdwa v92, v105, v56 dst_sel:DWORD dst_unused:UNUSED_PAD src0_sel:DWORD src1_sel:WORD_0
	v_add_u32_sdwa v93, v105, v56 dst_sel:DWORD dst_unused:UNUSED_PAD src0_sel:DWORD src1_sel:WORD_1
	v_add_u32_sdwa v106, v105, v57 dst_sel:DWORD dst_unused:UNUSED_PAD src0_sel:DWORD src1_sel:WORD_0
	v_add_u32_sdwa v107, v105, v57 dst_sel:DWORD dst_unused:UNUSED_PAD src0_sel:DWORD src1_sel:WORD_1
	v_add_u32_sdwa v108, v105, v58 dst_sel:DWORD dst_unused:UNUSED_PAD src0_sel:DWORD src1_sel:WORD_0
	v_add_u32_sdwa v109, v105, v58 dst_sel:DWORD dst_unused:UNUSED_PAD src0_sel:DWORD src1_sel:WORD_1
	v_add_u32_sdwa v88, v105, v59 dst_sel:DWORD dst_unused:UNUSED_PAD src0_sel:DWORD src1_sel:WORD_0
	v_add_u32_sdwa v89, v105, v59 dst_sel:DWORD dst_unused:UNUSED_PAD src0_sel:DWORD src1_sel:WORD_1
	ds_read_b128 v[120:123], v92
	ds_read_b128 v[124:127], v93
	ds_read_b128 v[128:131], v106
	ds_read_b128 v[132:135], v107
	ds_read_b128 v[140:143], v108
	ds_read_b128 v[144:147], v109
	ds_read_b128 v[148:151], v88
	ds_read_b128 v[152:155], v89
	v_add_u32_sdwa v88, v116, v42 dst_sel:DWORD dst_unused:UNUSED_PAD src0_sel:DWORD src1_sel:WORD_0
	v_add_u32_sdwa v89, v116, v42 dst_sel:DWORD dst_unused:UNUSED_PAD src0_sel:DWORD src1_sel:WORD_1
	v_add_u32_sdwa v90, v116, v43 dst_sel:DWORD dst_unused:UNUSED_PAD src0_sel:DWORD src1_sel:WORD_0
	v_add_u32_sdwa v91, v116, v43 dst_sel:DWORD dst_unused:UNUSED_PAD src0_sel:DWORD src1_sel:WORD_1
	v_bfe_u32 v117, v41, 16, 7
	v_add_u32_sdwa v118, v116, v39 dst_sel:DWORD dst_unused:UNUSED_PAD src0_sel:DWORD src1_sel:WORD_0
	v_add_u32_sdwa v119, v116, v39 dst_sel:DWORD dst_unused:UNUSED_PAD src0_sel:DWORD src1_sel:WORD_1
	v_add_u32_sdwa v136, v116, v41 dst_sel:DWORD dst_unused:UNUSED_PAD src0_sel:DWORD src1_sel:WORD_0
	s_and_b32 s10, s4, 0x600
	s_and_b32 s25, s21, 0x100
	s_or_b32 s10, s10, s25
	s_and_b32 s9, s4, 0xff
	s_cselect_b32 s24, 0, 0x700
	s_or_b32 s10, s10, s24
	s_waitcnt lgkmcnt(0)
	v_pk_add_f32 v[120:121], v[120:121], v[124:125]
	v_pk_add_f32 v[122:123], v[122:123], v[126:127]
	v_pk_add_f32 v[128:129], v[128:129], v[132:133]
	v_pk_add_f32 v[130:131], v[130:131], v[134:135]
	v_pk_add_f32 v[140:141], v[140:141], v[144:145]
	v_pk_add_f32 v[142:143], v[142:143], v[146:147]
	v_pk_add_f32 v[148:149], v[148:149], v[152:153]
	v_pk_add_f32 v[150:151], v[150:151], v[154:155]
	s_bitcmp1_b32 s4, 8
	s_cbranch_scc1 .Lfarslow_pre

.Lit_Af:
	ds_read_b64 v[68:69], v88
	ds_read_b64 v[70:71], v89
	ds_read_b64 v[72:73], v90
	ds_read_b64 v[74:75], v91
	v_add_u32_sdwa v92, v105, v52 dst_sel:DWORD dst_unused:UNUSED_PAD src0_sel:DWORD src1_sel:WORD_0
	v_add_u32_sdwa v93, v105, v52 dst_sel:DWORD dst_unused:UNUSED_PAD src0_sel:DWORD src1_sel:WORD_1
	v_add_u32_sdwa v106, v105, v53 dst_sel:DWORD dst_unused:UNUSED_PAD src0_sel:DWORD src1_sel:WORD_0
	v_add_u32_sdwa v107, v105, v53 dst_sel:DWORD dst_unused:UNUSED_PAD src0_sel:DWORD src1_sel:WORD_1
	v_add_u32_sdwa v108, v105, v54 dst_sel:DWORD dst_unused:UNUSED_PAD src0_sel:DWORD src1_sel:WORD_0
	v_add_u32_sdwa v109, v105, v54 dst_sel:DWORD dst_unused:UNUSED_PAD src0_sel:DWORD src1_sel:WORD_1
	v_add_u32_sdwa v88, v105, v55 dst_sel:DWORD dst_unused:UNUSED_PAD src0_sel:DWORD src1_sel:WORD_0
	v_add_u32_sdwa v89, v105, v55 dst_sel:DWORD dst_unused:UNUSED_PAD src0_sel:DWORD src1_sel:WORD_1
	ds_read_b128 v[120:123], v92
	ds_read_b128 v[124:127], v93
	ds_read_b128 v[128:131], v106
	ds_read_b128 v[132:135], v107
	ds_read_b128 v[140:143], v108
	ds_read_b128 v[144:147], v109
	ds_read_b128 v[148:151], v88
	ds_read_b128 v[152:155], v89
	s_waitcnt lgkmcnt(11)
	v_pk_add_f32 v[76:77], v[44:45], v[68:69]
	s_waitcnt lgkmcnt(9)
	v_pk_add_f32 v[78:79], v[70:71], v[72:73]
	s_waitcnt lgkmcnt(8)
	v_pk_add_f32 v[76:77], v[76:77], v[74:75]
	ds_read_b128 v[46:49], v138 offset:56896
	v_pk_add_f32 v[76:77], v[76:77], v[78:79]
	ds_read_b64 v[50:51], v139
	v_pk_mul_f32 v[78:79], v[40:41], v[76:77] op_sel_hi:[0,1]
	v_cmp_eq_u32_e64 s[6:7], 1, v117
	ds_write_b64 v137, v[78:79]
	ds_read2_b64 v[56:59], v156 offset1:2
	ds_read_b64 v[82:83], v118
	ds_read_b64 v[84:85], v119
	ds_read_b64 v[86:87], v136
	s_waitcnt lgkmcnt(6)
	v_pk_add_f32 v[120:121], v[120:121], v[124:125]
	v_pk_add_f32 v[122:123], v[122:123], v[126:127]
	v_pk_add_f32 v[128:129], v[128:129], v[132:133]
	v_pk_add_f32 v[130:131], v[130:131], v[134:135]
	v_pk_add_f32 v[140:141], v[140:141], v[144:145]
	v_pk_add_f32 v[142:143], v[142:143], v[146:147]
	v_pk_add_f32 v[148:149], v[148:149], v[152:153]
	v_pk_add_f32 v[150:151], v[150:151], v[154:155]
	v_pk_add_f32 v[120:121], v[120:121], v[128:129]
	v_pk_add_f32 v[122:123], v[122:123], v[130:131]
	v_pk_add_f32 v[140:141], v[140:141], v[148:149]
	v_pk_add_f32 v[142:143], v[142:143], v[150:151]
	v_pk_add_f32 v[120:121], v[120:121], v[140:141]
	v_pk_add_f32 v[122:123], v[122:123], v[142:143]
	v_add_u32_e32 v138, 0xfffffe00, v138
	v_add_u32_e32 v139, 0xffffff00, v139
	v_permlane32_swap_b32_e32 v120, v122
	v_permlane32_swap_b32_e32 v121, v123
	v_pk_add_f32 v[62:63], v[120:121], v[122:123]
	s_mov_b64 exec, s[6:7]
	s_waitcnt lgkmcnt(2)
	v_pk_fma_f32 v[80:81], v[40:41], v[82:83], v[78:79] op_sel_hi:[0,1,1]
	s_waitcnt lgkmcnt(1)
	v_pk_fma_f32 v[80:81], v[40:41], v[84:85], v[80:81] op_sel_hi:[0,1,1]
	s_waitcnt lgkmcnt(0)
	v_pk_fma_f32 v[80:81], v[40:41], v[86:87], v[80:81] op_sel_hi:[0,1,1]
	ds_write_b64 v137, v[80:81]
	s_mov_b64 exec, -1
	s_cmp_lt_u32 s9, 2
	s_cbranch_scc1 .Lnp_Af
	v_cmp_eq_u32_e64 s[6:7], 2, v117
	s_nop 0
	s_mov_b64 exec, s[6:7]
	ds_read_b64 v[82:83], v118
	ds_read_b64 v[84:85], v119
	ds_read_b64 v[86:87], v136
	s_mov_b64 exec, -1
	v_add_u32_sdwa v88, v116, v50 dst_sel:DWORD dst_unused:UNUSED_PAD src0_sel:DWORD src1_sel:WORD_0
	v_add_u32_sdwa v89, v116, v50 dst_sel:DWORD dst_unused:UNUSED_PAD src0_sel:DWORD src1_sel:WORD_1
	v_add_u32_sdwa v90, v116, v51 dst_sel:DWORD dst_unused:UNUSED_PAD src0_sel:DWORD src1_sel:WORD_0
	v_add_u32_sdwa v91, v116, v51 dst_sel:DWORD dst_unused:UNUSED_PAD src0_sel:DWORD src1_sel:WORD_1
	v_bfe_u32 v168, v49, 16, 7
	v_add_u32_sdwa v169, v116, v47 dst_sel:DWORD dst_unused:UNUSED_PAD src0_sel:DWORD src1_sel:WORD_0
	v_add_u32_sdwa v170, v116, v47 dst_sel:DWORD dst_unused:UNUSED_PAD src0_sel:DWORD src1_sel:WORD_1
	v_add_u32_sdwa v171, v116, v49 dst_sel:DWORD dst_unused:UNUSED_PAD src0_sel:DWORD src1_sel:WORD_0
	v_add_u32_e32 v156, 0xfffffa00, v156
	v_add_u32_e32 v172, 0xfffffe00, v137
	v_readlane_b32 s4, v60, s5
	v_max_i32_e32 v156, v156, v162
	v_lshl_add_u64 v[158:159], v[158:159], 0, s[2:3]
	s_and_b32 s10, s21, 0x600
	s_and_b32 s25, s4, 0x100
	s_or_b32 s10, s10, s25
	s_and_b32 s23, s21, 0xff
	s_cselect_b32 s24, 0, 0x700
	s_or_b32 s10, s10, s24
	s_mov_b64 exec, s[6:7]
	s_waitcnt lgkmcnt(2)
	v_pk_fma_f32 v[80:81], v[40:41], v[82:83], v[78:79] op_sel_hi:[0,1,1]
	s_waitcnt lgkmcnt(1)
	v_pk_fma_f32 v[80:81], v[40:41], v[84:85], v[80:81] op_sel_hi:[0,1,1]
	s_waitcnt lgkmcnt(0)
	v_pk_fma_f32 v[80:81], v[40:41], v[86:87], v[80:81] op_sel_hi:[0,1,1]
	ds_write_b64 v137, v[80:81]
	s_mov_b64 exec, -1
	s_cmp_lt_u32 s9, 3
	s_cbranch_scc1 .Lbot_A
	s_mov_b32 s8, 3

.Lit_Bf:
	ds_read_b64 v[68:69], v88
	ds_read_b64 v[70:71], v89
	ds_read_b64 v[72:73], v90
	ds_read_b64 v[74:75], v91
	v_add_u32_sdwa v92, v105, v56 dst_sel:DWORD dst_unused:UNUSED_PAD src0_sel:DWORD src1_sel:WORD_0
	v_add_u32_sdwa v93, v105, v56 dst_sel:DWORD dst_unused:UNUSED_PAD src0_sel:DWORD src1_sel:WORD_1
	v_add_u32_sdwa v106, v105, v57 dst_sel:DWORD dst_unused:UNUSED_PAD src0_sel:DWORD src1_sel:WORD_0
	v_add_u32_sdwa v107, v105, v57 dst_sel:DWORD dst_unused:UNUSED_PAD src0_sel:DWORD src1_sel:WORD_1
	v_add_u32_sdwa v108, v105, v58 dst_sel:DWORD dst_unused:UNUSED_PAD src0_sel:DWORD src1_sel:WORD_0
	v_add_u32_sdwa v109, v105, v58 dst_sel:DWORD dst_unused:UNUSED_PAD src0_sel:DWORD src1_sel:WORD_1
	v_add_u32_sdwa v88, v105, v59 dst_sel:DWORD dst_unused:UNUSED_PAD src0_sel:DWORD src1_sel:WORD_0
	v_add_u32_sdwa v89, v105, v59 dst_sel:DWORD dst_unused:UNUSED_PAD src0_sel:DWORD src1_sel:WORD_1
	ds_read_b128 v[120:123], v92
	ds_read_b128 v[124:127], v93
	ds_read_b128 v[128:131], v106
	ds_read_b128 v[132:135], v107
	ds_read_b128 v[140:143], v108
	ds_read_b128 v[144:147], v109
	ds_read_b128 v[148:151], v88
	ds_read_b128 v[152:155], v89
	s_waitcnt lgkmcnt(11)
	v_pk_add_f32 v[76:77], v[62:63], v[68:69]
	s_waitcnt lgkmcnt(9)
	v_pk_add_f32 v[78:79], v[70:71], v[72:73]
	s_waitcnt lgkmcnt(8)
	v_pk_add_f32 v[76:77], v[76:77], v[74:75]
	ds_read_b128 v[38:41], v138 offset:56896
	v_pk_add_f32 v[76:77], v[76:77], v[78:79]
	ds_read_b64 v[42:43], v139
	v_pk_mul_f32 v[78:79], v[48:49], v[76:77] op_sel_hi:[0,1]
	v_cmp_eq_u32_e64 s[6:7], 1, v168
	ds_write_b64 v172, v[78:79]
	ds_read2_b64 v[52:55], v156 offset1:2
	ds_read_b64 v[82:83], v169
	ds_read_b64 v[84:85], v170
	ds_read_b64 v[86:87], v171
	s_waitcnt lgkmcnt(6)
	v_pk_add_f32 v[120:121], v[120:121], v[124:125]
	v_pk_add_f32 v[122:123], v[122:123], v[126:127]
	v_pk_add_f32 v[128:129], v[128:129], v[132:133]
	v_pk_add_f32 v[130:131], v[130:131], v[134:135]
	v_pk_add_f32 v[140:141], v[140:141], v[144:145]
	v_pk_add_f32 v[142:143], v[142:143], v[146:147]
	v_pk_add_f32 v[148:149], v[148:149], v[152:153]
	v_pk_add_f32 v[150:151], v[150:151], v[154:155]
	v_pk_add_f32 v[120:121], v[120:121], v[128:129]
	v_pk_add_f32 v[122:123], v[122:123], v[130:131]
	v_pk_add_f32 v[140:141], v[140:141], v[148:149]
	v_pk_add_f32 v[142:143], v[142:143], v[150:151]
	v_pk_add_f32 v[120:121], v[120:121], v[140:141]
	v_pk_add_f32 v[122:123], v[122:123], v[142:143]
	v_add_u32_e32 v138, 0xfffffe00, v138
	v_add_u32_e32 v139, 0xffffff00, v139
	v_permlane32_swap_b32_e32 v120, v122
	v_permlane32_swap_b32_e32 v121, v123
	v_pk_add_f32 v[44:45], v[120:121], v[122:123]
	s_mov_b64 exec, s[6:7]
	s_waitcnt lgkmcnt(2)
	v_pk_fma_f32 v[80:81], v[48:49], v[82:83], v[78:79] op_sel_hi:[0,1,1]
	s_waitcnt lgkmcnt(1)
	v_pk_fma_f32 v[80:81], v[48:49], v[84:85], v[80:81] op_sel_hi:[0,1,1]
	s_waitcnt lgkmcnt(0)
	v_pk_fma_f32 v[80:81], v[48:49], v[86:87], v[80:81] op_sel_hi:[0,1,1]
	ds_write_b64 v172, v[80:81]
	s_mov_b64 exec, -1
	s_cmp_lt_u32 s23, 2
	s_cbranch_scc1 .Lnp_Bf
	v_cmp_eq_u32_e64 s[6:7], 2, v168
	s_nop 0
	s_mov_b64 exec, s[6:7]
	ds_read_b64 v[82:83], v169
	ds_read_b64 v[84:85], v170
	ds_read_b64 v[86:87], v171
	s_mov_b64 exec, -1
	v_add_u32_sdwa v88, v116, v42 dst_sel:DWORD dst_unused:UNUSED_PAD src0_sel:DWORD src1_sel:WORD_0
	v_add_u32_sdwa v89, v116, v42 dst_sel:DWORD dst_unused:UNUSED_PAD src0_sel:DWORD src1_sel:WORD_1
	v_add_u32_sdwa v90, v116, v43 dst_sel:DWORD dst_unused:UNUSED_PAD src0_sel:DWORD src1_sel:WORD_0
	v_add_u32_sdwa v91, v116, v43 dst_sel:DWORD dst_unused:UNUSED_PAD src0_sel:DWORD src1_sel:WORD_1
	v_bfe_u32 v117, v41, 16, 7
	v_add_u32_sdwa v118, v116, v39 dst_sel:DWORD dst_unused:UNUSED_PAD src0_sel:DWORD src1_sel:WORD_0
	v_add_u32_sdwa v119, v116, v39 dst_sel:DWORD dst_unused:UNUSED_PAD src0_sel:DWORD src1_sel:WORD_1
	v_add_u32_sdwa v136, v116, v41 dst_sel:DWORD dst_unused:UNUSED_PAD src0_sel:DWORD src1_sel:WORD_0
	v_add_u32_e32 v156, 0xfffffa00, v156
	v_add_u32_e32 v137, 0xfffffe00, v172
	v_readlane_b32 s21, v60, s5
	v_max_i32_e32 v156, v156, v162
	v_lshl_add_u64 v[158:159], v[158:159], 0, s[2:3]
	s_and_b32 s10, s4, 0x600
	s_and_b32 s25, s21, 0x100
	s_or_b32 s10, s10, s25
	s_and_b32 s9, s4, 0xff
	s_cselect_b32 s24, 0, 0x700
	s_or_b32 s10, s10, s24
	s_mov_b64 exec, s[6:7]
	s_waitcnt lgkmcnt(2)
	v_pk_fma_f32 v[80:81], v[48:49], v[82:83], v[78:79] op_sel_hi:[0,1,1]
	s_waitcnt lgkmcnt(1)
	v_pk_fma_f32 v[80:81], v[48:49], v[84:85], v[80:81] op_sel_hi:[0,1,1]
	s_waitcnt lgkmcnt(0)
	v_pk_fma_f32 v[80:81], v[48:49], v[86:87], v[80:81] op_sel_hi:[0,1,1]
	ds_write_b64 v172, v[80:81]
	s_mov_b64 exec, -1
	s_cmp_lt_u32 s23, 3
	s_cbranch_scc1 .Lbot_B
	s_mov_b32 s8, 3

.Lslowend_As:
	s_waitcnt lgkmcnt(0)
	v_add_u32_sdwa v88, v116, v50 dst_sel:DWORD dst_unused:UNUSED_PAD src0_sel:DWORD src1_sel:WORD_0
	v_add_u32_sdwa v89, v116, v50 dst_sel:DWORD dst_unused:UNUSED_PAD src0_sel:DWORD src1_sel:WORD_1
	v_add_u32_sdwa v90, v116, v51 dst_sel:DWORD dst_unused:UNUSED_PAD src0_sel:DWORD src1_sel:WORD_0
	v_add_u32_sdwa v91, v116, v51 dst_sel:DWORD dst_unused:UNUSED_PAD src0_sel:DWORD src1_sel:WORD_1
	v_bfe_u32 v168, v49, 16, 7
	v_add_u32_sdwa v169, v116, v47 dst_sel:DWORD dst_unused:UNUSED_PAD src0_sel:DWORD src1_sel:WORD_0
	v_add_u32_sdwa v170, v116, v47 dst_sel:DWORD dst_unused:UNUSED_PAD src0_sel:DWORD src1_sel:WORD_1
	v_add_u32_sdwa v171, v116, v49 dst_sel:DWORD dst_unused:UNUSED_PAD src0_sel:DWORD src1_sel:WORD_0
	v_add_u32_e32 v156, 0xfffffa00, v156
	v_add_u32_e32 v172, 0xfffffe00, v137
	v_readlane_b32 s4, v60, s5
	v_max_i32_e32 v156, v156, v162
	v_lshl_add_u64 v[158:159], v[158:159], 0, s[2:3]
	s_and_b32 s10, s21, 0x600
	s_and_b32 s25, s4, 0x100
	s_or_b32 s10, s10, s25
	s_and_b32 s23, s21, 0xff
	s_cselect_b32 s24, 0, 0x700
	s_or_b32 s10, s10, s24
	s_branch .Lbot_A

.Lslowend_Bs:
	s_waitcnt lgkmcnt(0)
	v_add_u32_sdwa v88, v116, v42 dst_sel:DWORD dst_unused:UNUSED_PAD src0_sel:DWORD src1_sel:WORD_0
	v_add_u32_sdwa v89, v116, v42 dst_sel:DWORD dst_unused:UNUSED_PAD src0_sel:DWORD src1_sel:WORD_1
	v_add_u32_sdwa v90, v116, v43 dst_sel:DWORD dst_unused:UNUSED_PAD src0_sel:DWORD src1_sel:WORD_0
	v_add_u32_sdwa v91, v116, v43 dst_sel:DWORD dst_unused:UNUSED_PAD src0_sel:DWORD src1_sel:WORD_1
	v_bfe_u32 v117, v41, 16, 7
	v_add_u32_sdwa v118, v116, v39 dst_sel:DWORD dst_unused:UNUSED_PAD src0_sel:DWORD src1_sel:WORD_0
	v_add_u32_sdwa v119, v116, v39 dst_sel:DWORD dst_unused:UNUSED_PAD src0_sel:DWORD src1_sel:WORD_1
	v_add_u32_sdwa v136, v116, v41 dst_sel:DWORD dst_unused:UNUSED_PAD src0_sel:DWORD src1_sel:WORD_0
	v_add_u32_e32 v156, 0xfffffa00, v156
	v_add_u32_e32 v137, 0xfffffe00, v172
	v_readlane_b32 s21, v60, s5
	v_max_i32_e32 v156, v156, v162
	v_lshl_add_u64 v[158:159], v[158:159], 0, s[2:3]
	s_and_b32 s10, s4, 0x600
	s_and_b32 s25, s21, 0x100
	s_or_b32 s10, s10, s25
	s_and_b32 s9, s4, 0xff
	s_cselect_b32 s24, 0, 0x700
	s_or_b32 s10, s10, s24
	s_branch .Lbot_B
.Lnp_Af:
	v_add_u32_sdwa v88, v116, v50 dst_sel:DWORD dst_unused:UNUSED_PAD src0_sel:DWORD src1_sel:WORD_0
	v_add_u32_sdwa v89, v116, v50 dst_sel:DWORD dst_unused:UNUSED_PAD src0_sel:DWORD src1_sel:WORD_1
	v_add_u32_sdwa v90, v116, v51 dst_sel:DWORD dst_unused:UNUSED_PAD src0_sel:DWORD src1_sel:WORD_0
	v_add_u32_sdwa v91, v116, v51 dst_sel:DWORD dst_unused:UNUSED_PAD src0_sel:DWORD src1_sel:WORD_1
	v_bfe_u32 v168, v49, 16, 7
	v_add_u32_sdwa v169, v116, v47 dst_sel:DWORD dst_unused:UNUSED_PAD src0_sel:DWORD src1_sel:WORD_0
	v_add_u32_sdwa v170, v116, v47 dst_sel:DWORD dst_unused:UNUSED_PAD src0_sel:DWORD src1_sel:WORD_1
	v_add_u32_sdwa v171, v116, v49 dst_sel:DWORD dst_unused:UNUSED_PAD src0_sel:DWORD src1_sel:WORD_0
	v_add_u32_e32 v156, 0xfffffa00, v156
	v_add_u32_e32 v172, 0xfffffe00, v137
	v_readlane_b32 s4, v60, s5
	v_max_i32_e32 v156, v156, v162
	v_lshl_add_u64 v[158:159], v[158:159], 0, s[2:3]
	s_and_b32 s10, s21, 0x600
	s_and_b32 s25, s4, 0x100
	s_or_b32 s10, s10, s25
	s_and_b32 s23, s21, 0xff
	s_cselect_b32 s24, 0, 0x700
	s_or_b32 s10, s10, s24
	s_branch .Lbot_A
.Lnp_Bf:
	v_add_u32_sdwa v88, v116, v42 dst_sel:DWORD dst_unused:UNUSED_PAD src0_sel:DWORD src1_sel:WORD_0
	v_add_u32_sdwa v89, v116, v42 dst_sel:DWORD dst_unused:UNUSED_PAD src0_sel:DWORD src1_sel:WORD_1
	v_add_u32_sdwa v90, v116, v43 dst_sel:DWORD dst_unused:UNUSED_PAD src0_sel:DWORD src1_sel:WORD_0
	v_add_u32_sdwa v91, v116, v43 dst_sel:DWORD dst_unused:UNUSED_PAD src0_sel:DWORD src1_sel:WORD_1
	v_bfe_u32 v117, v41, 16, 7
	v_add_u32_sdwa v118, v116, v39 dst_sel:DWORD dst_unused:UNUSED_PAD src0_sel:DWORD src1_sel:WORD_0
	v_add_u32_sdwa v119, v116, v39 dst_sel:DWORD dst_unused:UNUSED_PAD src0_sel:DWORD src1_sel:WORD_1
	v_add_u32_sdwa v136, v116, v41 dst_sel:DWORD dst_unused:UNUSED_PAD src0_sel:DWORD src1_sel:WORD_0
	v_add_u32_e32 v156, 0xfffffa00, v156
	v_add_u32_e32 v137, 0xfffffe00, v172
	v_readlane_b32 s21, v60, s5
	v_max_i32_e32 v156, v156, v162
	v_lshl_add_u64 v[158:159], v[158:159], 0, s[2:3]
	s_and_b32 s10, s4, 0x600
	s_and_b32 s25, s21, 0x100
	s_or_b32 s10, s10, s25
	s_and_b32 s9, s4, 0xff
	s_cselect_b32 s24, 0, 0x700
	s_or_b32 s10, s10, s24
	s_branch .Lbot_B
